# attention step: all 16 K/Q fragment reads issued up front into freed registers, V transposed reads hoisted before/inside softmax (PV MFMAs no longer wait on LDS)
# speedup vs baseline: 1.0024x; 1.0024x over previous
.LBB0_725:
	s_ashr_i32 s68, s73, 31
	s_lshr_b32 s68, s68, 26
	s_add_i32 s79, s73, s68
	s_add_i32 s81, s73, -4
	s_and_b32 s68, s79, 0xffffffc0
	s_max_i32 s68, s81, s68
	s_cmp_lt_i32 s72, s68
	s_cselect_b64 vcc, -1, 0
	s_or_b64 s[84:85], s[84:85], vcc
	s_cmp_gt_i32 s72, s73
	s_cselect_b64 vcc, -1, 0
	s_or_b64 vcc, vcc, s[84:85]
	s_mov_b64 s[84:85], -1
	s_and_b64 vcc, exec, vcc
	v_add_u32_e32 v219, v172, v175
	v_add_u32_e32 v224, v172, v176
	v_add_u32_e32 v225, v172, v177
	v_add_u32_e32 v226, v172, v178
	v_add_u32_e32 v227, v172, v180
	v_add_u32_e32 v228, v172, v181
	v_add_u32_e32 v229, v172, v182
	v_add_u32_e32 v230, v172, v183
	s_cbranch_vccnz .LBB0_734
	s_mul_i32 s68, s72, 0xcd
	s_bfe_u32 s68, s68, 0x6000a
	s_mul_i32 s68, s68, 5
	s_sub_i32 s68, s72, s68
	s_and_b32 s68, s68, 0xff
	s_lshl_b32 s68, s68, 14
	s_add_i32 s80, s68, 0
	v_add_u32_e32 v220, s80, v171
	v_add_u32_e32 v221, v220, v175
	ds_read_b128 v[66:69], v221
	ds_read_b128 v[98:101], v219
	v_add_u32_e32 v222, v220, v176
	ds_read_b128 v[70:73], v222
	ds_read_b128 v[102:105], v224
	v_add_u32_e32 v221, v220, v177
	ds_read_b128 v[74:77], v221
	ds_read_b128 v[106:109], v225
	v_add_u32_e32 v222, v220, v178
	ds_read_b128 v[78:81], v222
	ds_read_b128 v[110:113], v226
	v_add_u32_e32 v221, v220, v180
	ds_read_b128 v[82:85], v221
	ds_read_b128 v[114:117], v227
	v_add_u32_e32 v222, v220, v181
	ds_read_b128 v[86:89], v222
	ds_read_b128 v[118:121], v228
	s_waitcnt lgkmcnt(10)
	v_mfma_f32_32x32x16_bf16 v[130:145], v[66:69], v[98:101], 0
	v_add_u32_e32 v221, v220, v182
	ds_read_b128 v[90:93], v221
	ds_read_b128 v[122:125], v229
	s_waitcnt lgkmcnt(10)
	v_mfma_f32_32x32x16_bf16 v[130:145], v[70:73], v[102:105], v[130:145]
	v_add_u32_e32 v222, v220, v183
	ds_read_b128 v[94:97], v222
	ds_read_b128 v[126:129], v230
	s_waitcnt lgkmcnt(10)
	v_mfma_f32_32x32x16_bf16 v[130:145], v[74:77], v[106:109], v[130:145]
	s_waitcnt lgkmcnt(8)
	v_mfma_f32_32x32x16_bf16 v[130:145], v[78:81], v[110:113], v[130:145]
	s_waitcnt lgkmcnt(6)
	v_mfma_f32_32x32x16_bf16 v[130:145], v[82:85], v[114:117], v[130:145]
	s_waitcnt lgkmcnt(4)
	v_mfma_f32_32x32x16_bf16 v[130:145], v[86:89], v[118:121], v[130:145]
	s_waitcnt lgkmcnt(2)
	v_mfma_f32_32x32x16_bf16 v[130:145], v[90:93], v[122:125], v[130:145]
	s_cmp_lg_u32 s72, s81
	s_waitcnt lgkmcnt(0)
	v_mfma_f32_32x32x16_bf16 v[130:145], v[94:97], v[126:129], v[130:145]
	v_add_u32_e32 v69, s80, v173
	v_add3_u32 v70, v69, v185, v186
	ds_read_b64_tr_b16 v[98:99], v70 offset:8192
	v_add3_u32 v71, v69, v187, v188
	ds_read_b64_tr_b16 v[100:101], v71 offset:8192
	v_add3_u32 v70, v69, v185, v191
	ds_read_b64_tr_b16 v[102:103], v70 offset:8192
	v_add3_u32 v71, v69, v187, v192
	ds_read_b64_tr_b16 v[104:105], v71 offset:8192
	v_add3_u32 v70, v69, v184, v186
	ds_read_b64_tr_b16 v[106:107], v70 offset:8192
	v_add3_u32 v71, v69, v189, v190
	ds_read_b64_tr_b16 v[108:109], v71 offset:8192
	v_add3_u32 v70, v69, v184, v191
	ds_read_b64_tr_b16 v[110:111], v70 offset:8192
	v_add3_u32 v71, v69, v189, v193
	ds_read_b64_tr_b16 v[112:113], v71 offset:8192
	s_cbranch_scc1 .LBB0_728
	s_nop 10
	v_cndmask_b32_e64 v130, v130, v216, s[4:5]
	v_cndmask_b32_e64 v131, v131, v216, s[6:7]
	v_cndmask_b32_e64 v132, v132, v216, s[8:9]
	v_cndmask_b32_e64 v133, v133, v216, s[10:11]
	v_cndmask_b32_e64 v134, v134, v216, s[12:13]
	v_cndmask_b32_e64 v135, v135, v216, s[14:15]
	v_cndmask_b32_e64 v136, v136, v216, s[16:17]
	v_cndmask_b32_e64 v137, v137, v216, s[18:19]
	v_cndmask_b32_e64 v138, v138, v216, s[20:21]
	v_cndmask_b32_e64 v139, v139, v216, s[22:23]
	v_cndmask_b32_e64 v140, v140, v216, s[24:25]
	v_cndmask_b32_e64 v141, v141, v216, s[26:27]
	v_cndmask_b32_e64 v142, v142, v216, s[28:29]
	v_cndmask_b32_e64 v143, v143, v216, s[30:31]
	v_cndmask_b32_e64 v144, v144, v216, s[34:35]
	v_cndmask_b32_e64 v145, v145, v216, s[36:37]

.LBB0_730:
	s_nop 6
	v_max_f32_e32 v66, v131, v131
	v_max_f32_e32 v67, v130, v130
	v_max_f32_e32 v66, v67, v66
	v_max3_f32 v66, v66, v132, v133
	v_max3_f32 v66, v66, v134, v135
	v_max3_f32 v66, v66, v136, v137
	v_and_b32_e32 v68, 64, v166
	v_max3_f32 v66, v66, v138, v139
	v_xor_b32_e32 v67, 32, v166
	v_add_u32_e32 v68, 64, v68
	v_max3_f32 v66, v66, v140, v141
	v_cmp_lt_i32_e32 vcc, v67, v68
	v_max3_f32 v66, v66, v142, v143
	v_max3_f32 v66, v66, v144, v145
	v_cndmask_b32_e32 v67, v166, v67, vcc
	v_lshlrev_b32_e32 v67, 2, v67
	ds_bpermute_b32 v67, v67, v66
	s_waitcnt lgkmcnt(0)
	v_add3_u32 v70, v69, v185, v194
	ds_read_b64_tr_b16 v[114:115], v70 offset:8192
	v_add3_u32 v71, v69, v187, v195
	ds_read_b64_tr_b16 v[116:117], v71 offset:8192
	v_add3_u32 v70, v69, v185, v197
	ds_read_b64_tr_b16 v[118:119], v70 offset:8192
	v_add3_u32 v71, v69, v187, v198
	ds_read_b64_tr_b16 v[120:121], v71 offset:8192
	v_add3_u32 v70, v69, v184, v194
	ds_read_b64_tr_b16 v[122:123], v70 offset:8192
	v_add3_u32 v71, v69, v189, v196
	ds_read_b64_tr_b16 v[124:125], v71 offset:8192
	v_add3_u32 v70, v69, v184, v197
	ds_read_b64_tr_b16 v[126:127], v70 offset:8192
	v_add3_u32 v71, v69, v189, v199
	ds_read_b64_tr_b16 v[128:129], v71 offset:8192
	v_max_f32_e32 v67, v67, v67
	v_max_f32_e32 v66, v66, v67
	v_add_f32_e32 v67, 0x40c00000, v231
	v_cmp_gt_f32_e32 vcc, v66, v67
	s_nop 1
	v_cndmask_b32_e32 v233, v231, v66, vcc
	v_sub_f32_e32 v66, v231, v233
	v_exp_f32_e32 v146, v66
	s_cbranch_vccz .LBB0_732
	v_pk_mul_f32 v[64:65], v[64:65], v[146:147] op_sel_hi:[1,0]
	v_pk_mul_f32 v[62:63], v[62:63], v[146:147] op_sel_hi:[1,0]
	v_pk_mul_f32 v[60:61], v[60:61], v[146:147] op_sel_hi:[1,0]
	v_pk_mul_f32 v[58:59], v[58:59], v[146:147] op_sel_hi:[1,0]
	v_pk_mul_f32 v[56:57], v[56:57], v[146:147] op_sel_hi:[1,0]
	v_pk_mul_f32 v[54:55], v[54:55], v[146:147] op_sel_hi:[1,0]
	v_pk_mul_f32 v[52:53], v[52:53], v[146:147] op_sel_hi:[1,0]
	v_pk_mul_f32 v[50:51], v[50:51], v[146:147] op_sel_hi:[1,0]
	v_pk_mul_f32 v[48:49], v[48:49], v[146:147] op_sel_hi:[1,0]
	v_pk_mul_f32 v[46:47], v[46:47], v[146:147] op_sel_hi:[1,0]
	v_pk_mul_f32 v[44:45], v[44:45], v[146:147] op_sel_hi:[1,0]
	v_pk_mul_f32 v[42:43], v[42:43], v[146:147] op_sel_hi:[1,0]
	v_pk_mul_f32 v[40:41], v[40:41], v[146:147] op_sel_hi:[1,0]
	v_pk_mul_f32 v[38:39], v[38:39], v[146:147] op_sel_hi:[1,0]
	v_pk_mul_f32 v[36:37], v[36:37], v[146:147] op_sel_hi:[1,0]
	v_pk_mul_f32 v[34:35], v[34:35], v[146:147] op_sel_hi:[1,0]
	v_pk_mul_f32 v[32:33], v[32:33], v[146:147] op_sel_hi:[1,0]
	v_pk_mul_f32 v[30:31], v[30:31], v[146:147] op_sel_hi:[1,0]
	v_pk_mul_f32 v[28:29], v[28:29], v[146:147] op_sel_hi:[1,0]
	v_pk_mul_f32 v[26:27], v[26:27], v[146:147] op_sel_hi:[1,0]
	v_pk_mul_f32 v[24:25], v[24:25], v[146:147] op_sel_hi:[1,0]
	v_pk_mul_f32 v[22:23], v[22:23], v[146:147] op_sel_hi:[1,0]
	v_pk_mul_f32 v[20:21], v[20:21], v[146:147] op_sel_hi:[1,0]
	v_pk_mul_f32 v[18:19], v[18:19], v[146:147] op_sel_hi:[1,0]
	v_pk_mul_f32 v[16:17], v[16:17], v[146:147] op_sel_hi:[1,0]
	v_pk_mul_f32 v[14:15], v[14:15], v[146:147] op_sel_hi:[1,0]
	v_pk_mul_f32 v[12:13], v[12:13], v[146:147] op_sel_hi:[1,0]
	v_pk_mul_f32 v[10:11], v[10:11], v[146:147] op_sel_hi:[1,0]
	v_pk_mul_f32 v[8:9], v[8:9], v[146:147] op_sel_hi:[1,0]
	v_pk_mul_f32 v[6:7], v[6:7], v[146:147] op_sel_hi:[1,0]
	v_pk_mul_f32 v[4:5], v[4:5], v[146:147] op_sel_hi:[1,0]
	v_pk_mul_f32 v[2:3], v[2:3], v[146:147] op_sel_hi:[1,0]
	s_branch .LBB0_733
.LBB0_732:
.LBB0_733:
	v_sub_f32_e32 v130, v130, v233
	v_exp_f32_e32 v130, v130
	v_sub_f32_e32 v131, v131, v233
	v_exp_f32_e32 v131, v131
	v_sub_f32_e32 v132, v132, v233
	v_exp_f32_e32 v132, v132
	v_sub_f32_e32 v133, v133, v233
	v_exp_f32_e32 v133, v133
	v_sub_f32_e32 v134, v134, v233
	v_add_f32_e32 v220, 0, v130
	v_exp_f32_e32 v221, v134
	v_add_f32_e32 v220, v131, v220
	v_add_f32_e32 v220, v132, v220
	v_sub_f32_e32 v135, v135, v233
	v_add_f32_e32 v220, v133, v220
	v_exp_f32_e32 v135, v135
	v_sub_f32_e32 v136, v136, v233
	v_add_f32_e32 v134, v221, v220
	v_exp_f32_e32 v220, v136
	v_sub_f32_e32 v136, v137, v233
	v_exp_f32_e32 v222, v136
	v_sub_f32_e32 v136, v138, v233
	v_exp_f32_e32 v223, v136
	v_sub_f32_e32 v136, v139, v233
	v_add_f32_e32 v134, v135, v134
	v_exp_f32_e32 v234, v136
	v_sub_f32_e32 v136, v140, v233
	v_add_f32_e32 v134, v220, v134
	v_exp_f32_e32 v140, v136
	v_sub_f32_e32 v136, v141, v233
	v_add_f32_e32 v134, v222, v134
	v_exp_f32_e32 v141, v136
	v_sub_f32_e32 v136, v142, v233
	v_add_f32_e32 v134, v223, v134
	v_exp_f32_e32 v142, v136
	v_sub_f32_e32 v136, v143, v233
	v_add_f32_e32 v134, v234, v134
	v_exp_f32_e32 v143, v136
	v_sub_f32_e32 v136, v144, v233
	v_add_f32_e32 v134, v140, v134
	v_exp_f32_e32 v144, v136
	v_sub_f32_e32 v136, v145, v233
	v_add_f32_e32 v134, v141, v134
	v_exp_f32_e32 v145, v136
	v_add_f32_e32 v134, v142, v134
	v_add_f32_e32 v134, v143, v134
	v_add_f32_e32 v134, v144, v134
	v_add_f32_e32 v134, v145, v134
	v_cvt_pk_bf16_f32 v136, v130, v131
	v_cvt_pk_bf16_f32 v137, v132, v133
	v_cvt_pk_bf16_f32 v138, v221, v135
	v_cvt_pk_bf16_f32 v139, v220, v222
	v_cvt_pk_bf16_f32 v130, v223, v234
	v_cvt_pk_bf16_f32 v131, v140, v141
	v_cvt_pk_bf16_f32 v132, v142, v143
	v_cvt_pk_bf16_f32 v133, v144, v145
	v_fmac_f32_e32 v134, v232, v146
	s_nop 1
	s_waitcnt lgkmcnt(8)
	v_mfma_f32_32x32x16_bf16 v[50:65], v[98:101], v[136:139], v[50:65]
	s_waitcnt lgkmcnt(8)
	v_mfma_f32_32x32x16_bf16 v[34:49], v[102:105], v[136:139], v[34:49]
	s_waitcnt lgkmcnt(8)
	v_mfma_f32_32x32x16_bf16 v[50:65], v[106:109], v[130:133], v[50:65]
	s_waitcnt lgkmcnt(8)
	v_mfma_f32_32x32x16_bf16 v[34:49], v[110:113], v[130:133], v[34:49]
	s_waitcnt lgkmcnt(6)
	v_mfma_f32_32x32x16_bf16 v[18:33], v[114:117], v[136:139], v[18:33]
	s_waitcnt lgkmcnt(4)
	v_mfma_f32_32x32x16_bf16 v[2:17], v[118:121], v[136:139], v[2:17]
	s_waitcnt lgkmcnt(2)
	v_mfma_f32_32x32x16_bf16 v[18:33], v[122:125], v[130:133], v[18:33]
	s_waitcnt lgkmcnt(0)
	v_mfma_f32_32x32x16_bf16 v[2:17], v[126:129], v[130:133], v[2:17]
	s_and_b64 s[80:81], s[84:85], exec
	s_cselect_b32 s80, 0, s78
	s_mov_b64 s[84:85], 0

.LBB0_795:
	s_ashr_i32 s68, s73, 31
	s_lshr_b32 s68, s68, 28
	s_add_i32 s79, s73, s68
	s_add_i32 s81, s73, -4
	s_and_b32 s68, s79, -16
	s_max_i32 s68, s81, s68
	s_cmp_lt_i32 s87, s68
	s_cselect_b64 vcc, -1, 0
	s_or_b64 s[84:85], s[84:85], vcc
	s_cmp_gt_i32 s87, s73
	s_cselect_b64 vcc, -1, 0
	s_or_b64 vcc, vcc, s[84:85]
	s_mov_b64 s[84:85], -1
	s_and_b64 vcc, exec, vcc
	s_cbranch_vccnz .LBB0_804
	s_mul_i32 s68, s87, 0xcd
	s_bfe_u32 s68, s68, 0x6000a
	s_mul_i32 s68, s68, 5
	s_sub_i32 s68, s87, s68
	s_and_b32 s68, s68, 0xff
	s_lshl_b32 s68, s68, 14
	s_add_i32 s80, s68, 0
	v_add_u32_e32 v220, s80, v171
	v_add_u32_e32 v221, v220, v175
	ds_read_b128 v[66:69], v221
	ds_read_b128 v[98:101], v219
	v_add_u32_e32 v222, v220, v176
	ds_read_b128 v[70:73], v222
	ds_read_b128 v[102:105], v224
	v_add_u32_e32 v221, v220, v177
	ds_read_b128 v[74:77], v221
	ds_read_b128 v[106:109], v225
	v_add_u32_e32 v222, v220, v178
	ds_read_b128 v[78:81], v222
	ds_read_b128 v[110:113], v226
	v_add_u32_e32 v221, v220, v180
	ds_read_b128 v[82:85], v221
	ds_read_b128 v[114:117], v227
	v_add_u32_e32 v222, v220, v181
	ds_read_b128 v[86:89], v222
	ds_read_b128 v[118:121], v228
	s_waitcnt lgkmcnt(10)
	v_mfma_f32_32x32x16_bf16 v[130:145], v[66:69], v[98:101], 0
	v_add_u32_e32 v221, v220, v182
	ds_read_b128 v[90:93], v221
	ds_read_b128 v[122:125], v229
	s_waitcnt lgkmcnt(10)
	v_mfma_f32_32x32x16_bf16 v[130:145], v[70:73], v[102:105], v[130:145]
	v_add_u32_e32 v222, v220, v183
	ds_read_b128 v[94:97], v222
	ds_read_b128 v[126:129], v230
	s_waitcnt lgkmcnt(10)
	v_mfma_f32_32x32x16_bf16 v[130:145], v[74:77], v[106:109], v[130:145]
	s_waitcnt lgkmcnt(8)
	v_mfma_f32_32x32x16_bf16 v[130:145], v[78:81], v[110:113], v[130:145]
	s_waitcnt lgkmcnt(6)
	v_mfma_f32_32x32x16_bf16 v[130:145], v[82:85], v[114:117], v[130:145]
	s_waitcnt lgkmcnt(4)
	v_mfma_f32_32x32x16_bf16 v[130:145], v[86:89], v[118:121], v[130:145]
	s_waitcnt lgkmcnt(2)
	v_mfma_f32_32x32x16_bf16 v[130:145], v[90:93], v[122:125], v[130:145]
	s_cmp_lg_u32 s87, s81
	s_waitcnt lgkmcnt(0)
	v_mfma_f32_32x32x16_bf16 v[130:145], v[94:97], v[126:129], v[130:145]
	v_add_u32_e32 v69, s80, v173
	v_add3_u32 v70, v69, v185, v186
	ds_read_b64_tr_b16 v[98:99], v70 offset:8192
	v_add3_u32 v71, v69, v187, v188
	ds_read_b64_tr_b16 v[100:101], v71 offset:8192
	v_add3_u32 v70, v69, v185, v191
	ds_read_b64_tr_b16 v[102:103], v70 offset:8192
	v_add3_u32 v71, v69, v187, v192
	ds_read_b64_tr_b16 v[104:105], v71 offset:8192
	v_add3_u32 v70, v69, v184, v186
	ds_read_b64_tr_b16 v[106:107], v70 offset:8192
	v_add3_u32 v71, v69, v189, v190
	ds_read_b64_tr_b16 v[108:109], v71 offset:8192
	v_add3_u32 v70, v69, v184, v191
	ds_read_b64_tr_b16 v[110:111], v70 offset:8192
	v_add3_u32 v71, v69, v189, v193
	ds_read_b64_tr_b16 v[112:113], v71 offset:8192
	s_cbranch_scc1 .LBB0_798
	s_nop 10
	v_cndmask_b32_e64 v130, v130, v216, s[4:5]
	v_cndmask_b32_e64 v131, v131, v216, s[6:7]
	v_cndmask_b32_e64 v132, v132, v216, s[8:9]
	v_cndmask_b32_e64 v133, v133, v216, s[10:11]
	v_cndmask_b32_e64 v134, v134, v216, s[12:13]
	v_cndmask_b32_e64 v135, v135, v216, s[14:15]
	v_cndmask_b32_e64 v136, v136, v216, s[16:17]
	v_cndmask_b32_e64 v137, v137, v216, s[18:19]
	v_cndmask_b32_e64 v138, v138, v216, s[20:21]
	v_cndmask_b32_e64 v139, v139, v216, s[22:23]
	v_cndmask_b32_e64 v140, v140, v216, s[24:25]
	v_cndmask_b32_e64 v141, v141, v216, s[26:27]
	v_cndmask_b32_e64 v142, v142, v216, s[28:29]
	v_cndmask_b32_e64 v143, v143, v216, s[30:31]
	v_cndmask_b32_e64 v144, v144, v216, s[34:35]
	v_cndmask_b32_e64 v145, v145, v216, s[36:37]

.LBB0_800:
	s_nop 6
	v_max_f32_e32 v66, v131, v131
	v_max_f32_e32 v67, v130, v130
	v_max_f32_e32 v66, v67, v66
	v_max3_f32 v66, v66, v132, v133
	v_max3_f32 v66, v66, v134, v135
	v_max3_f32 v66, v66, v136, v137
	v_and_b32_e32 v68, 64, v166
	v_max3_f32 v66, v66, v138, v139
	v_xor_b32_e32 v67, 32, v166
	v_add_u32_e32 v68, 64, v68
	v_max3_f32 v66, v66, v140, v141
	v_cmp_lt_i32_e32 vcc, v67, v68
	v_max3_f32 v66, v66, v142, v143
	v_max3_f32 v66, v66, v144, v145
	v_cndmask_b32_e32 v67, v166, v67, vcc
	v_lshlrev_b32_e32 v67, 2, v67
	ds_bpermute_b32 v67, v67, v66
	s_waitcnt lgkmcnt(0)
	v_add3_u32 v70, v69, v185, v194
	ds_read_b64_tr_b16 v[114:115], v70 offset:8192
	v_add3_u32 v71, v69, v187, v195
	ds_read_b64_tr_b16 v[116:117], v71 offset:8192
	v_add3_u32 v70, v69, v185, v197
	ds_read_b64_tr_b16 v[118:119], v70 offset:8192
	v_add3_u32 v71, v69, v187, v198
	ds_read_b64_tr_b16 v[120:121], v71 offset:8192
	v_add3_u32 v70, v69, v184, v194
	ds_read_b64_tr_b16 v[122:123], v70 offset:8192
	v_add3_u32 v71, v69, v189, v196
	ds_read_b64_tr_b16 v[124:125], v71 offset:8192
	v_add3_u32 v70, v69, v184, v197
	ds_read_b64_tr_b16 v[126:127], v70 offset:8192
	v_add3_u32 v71, v69, v189, v199
	ds_read_b64_tr_b16 v[128:129], v71 offset:8192
	v_max_f32_e32 v67, v67, v67
	v_max_f32_e32 v66, v66, v67
	v_add_f32_e32 v67, 0x40c00000, v233
	v_cmp_gt_f32_e32 vcc, v66, v67
	s_nop 1
	v_cndmask_b32_e32 v235, v233, v66, vcc
	v_sub_f32_e32 v66, v233, v235
	v_exp_f32_e32 v146, v66
	s_cbranch_vccz .LBB0_802
	v_pk_mul_f32 v[64:65], v[64:65], v[146:147] op_sel_hi:[1,0]
	v_pk_mul_f32 v[62:63], v[62:63], v[146:147] op_sel_hi:[1,0]
	v_pk_mul_f32 v[60:61], v[60:61], v[146:147] op_sel_hi:[1,0]
	v_pk_mul_f32 v[58:59], v[58:59], v[146:147] op_sel_hi:[1,0]
	v_pk_mul_f32 v[56:57], v[56:57], v[146:147] op_sel_hi:[1,0]
	v_pk_mul_f32 v[54:55], v[54:55], v[146:147] op_sel_hi:[1,0]
	v_pk_mul_f32 v[52:53], v[52:53], v[146:147] op_sel_hi:[1,0]
	v_pk_mul_f32 v[50:51], v[50:51], v[146:147] op_sel_hi:[1,0]
	v_pk_mul_f32 v[48:49], v[48:49], v[146:147] op_sel_hi:[1,0]
	v_pk_mul_f32 v[46:47], v[46:47], v[146:147] op_sel_hi:[1,0]
	v_pk_mul_f32 v[44:45], v[44:45], v[146:147] op_sel_hi:[1,0]
	v_pk_mul_f32 v[42:43], v[42:43], v[146:147] op_sel_hi:[1,0]
	v_pk_mul_f32 v[40:41], v[40:41], v[146:147] op_sel_hi:[1,0]
	v_pk_mul_f32 v[38:39], v[38:39], v[146:147] op_sel_hi:[1,0]
	v_pk_mul_f32 v[36:37], v[36:37], v[146:147] op_sel_hi:[1,0]
	v_pk_mul_f32 v[34:35], v[34:35], v[146:147] op_sel_hi:[1,0]
	v_pk_mul_f32 v[32:33], v[32:33], v[146:147] op_sel_hi:[1,0]
	v_pk_mul_f32 v[30:31], v[30:31], v[146:147] op_sel_hi:[1,0]
	v_pk_mul_f32 v[28:29], v[28:29], v[146:147] op_sel_hi:[1,0]
	v_pk_mul_f32 v[26:27], v[26:27], v[146:147] op_sel_hi:[1,0]
	v_pk_mul_f32 v[24:25], v[24:25], v[146:147] op_sel_hi:[1,0]
	v_pk_mul_f32 v[22:23], v[22:23], v[146:147] op_sel_hi:[1,0]
	v_pk_mul_f32 v[20:21], v[20:21], v[146:147] op_sel_hi:[1,0]
	v_pk_mul_f32 v[18:19], v[18:19], v[146:147] op_sel_hi:[1,0]
	v_pk_mul_f32 v[16:17], v[16:17], v[146:147] op_sel_hi:[1,0]
	v_pk_mul_f32 v[14:15], v[14:15], v[146:147] op_sel_hi:[1,0]
	v_pk_mul_f32 v[12:13], v[12:13], v[146:147] op_sel_hi:[1,0]
	v_pk_mul_f32 v[10:11], v[10:11], v[146:147] op_sel_hi:[1,0]
	v_pk_mul_f32 v[8:9], v[8:9], v[146:147] op_sel_hi:[1,0]
	v_pk_mul_f32 v[6:7], v[6:7], v[146:147] op_sel_hi:[1,0]
	v_pk_mul_f32 v[4:5], v[4:5], v[146:147] op_sel_hi:[1,0]
	v_pk_mul_f32 v[2:3], v[2:3], v[146:147] op_sel_hi:[1,0]
	s_branch .LBB0_803
.LBB0_802:
.LBB0_803:
	v_sub_f32_e32 v130, v130, v235
	v_exp_f32_e32 v130, v130
	v_sub_f32_e32 v131, v131, v235
	v_exp_f32_e32 v131, v131
	v_sub_f32_e32 v132, v132, v235
	v_exp_f32_e32 v132, v132
	v_sub_f32_e32 v133, v133, v235
	v_exp_f32_e32 v133, v133
	v_sub_f32_e32 v134, v134, v235
	v_add_f32_e32 v220, 0, v130
	v_exp_f32_e32 v221, v134
	v_add_f32_e32 v220, v131, v220
	v_add_f32_e32 v220, v132, v220
	v_sub_f32_e32 v135, v135, v235
	v_add_f32_e32 v220, v133, v220
	v_exp_f32_e32 v135, v135
	v_sub_f32_e32 v136, v136, v235
	v_add_f32_e32 v134, v221, v220
	v_exp_f32_e32 v220, v136
	v_sub_f32_e32 v136, v137, v235
	v_exp_f32_e32 v222, v136
	v_sub_f32_e32 v136, v138, v235
	v_exp_f32_e32 v223, v136
	v_sub_f32_e32 v136, v139, v235
	v_add_f32_e32 v134, v135, v134
	v_exp_f32_e32 v236, v136
	v_sub_f32_e32 v136, v140, v235
	v_add_f32_e32 v134, v220, v134
	v_exp_f32_e32 v140, v136
	v_sub_f32_e32 v136, v141, v235
	v_add_f32_e32 v134, v222, v134
	v_exp_f32_e32 v141, v136
	v_sub_f32_e32 v136, v142, v235
	v_add_f32_e32 v134, v223, v134
	v_exp_f32_e32 v142, v136
	v_sub_f32_e32 v136, v143, v235
	v_add_f32_e32 v134, v236, v134
	v_exp_f32_e32 v143, v136
	v_sub_f32_e32 v136, v144, v235
	v_add_f32_e32 v134, v140, v134
	v_exp_f32_e32 v144, v136
	v_sub_f32_e32 v136, v145, v235
	v_add_f32_e32 v134, v141, v134
	v_exp_f32_e32 v145, v136
	v_add_f32_e32 v134, v142, v134
	v_add_f32_e32 v134, v143, v134
	v_add_f32_e32 v134, v144, v134
	v_add_f32_e32 v134, v145, v134
	v_cvt_pk_bf16_f32 v136, v130, v131
	v_cvt_pk_bf16_f32 v137, v132, v133
	v_cvt_pk_bf16_f32 v138, v221, v135
	v_cvt_pk_bf16_f32 v139, v220, v222
	v_cvt_pk_bf16_f32 v130, v223, v236
	v_cvt_pk_bf16_f32 v131, v140, v141
	v_cvt_pk_bf16_f32 v132, v142, v143
	v_cvt_pk_bf16_f32 v133, v144, v145
	v_fmac_f32_e32 v134, v234, v146
	s_nop 1
	s_waitcnt lgkmcnt(8)
	v_mfma_f32_32x32x16_bf16 v[50:65], v[98:101], v[136:139], v[50:65]
	s_waitcnt lgkmcnt(8)
	v_mfma_f32_32x32x16_bf16 v[34:49], v[102:105], v[136:139], v[34:49]
	s_waitcnt lgkmcnt(8)
	v_mfma_f32_32x32x16_bf16 v[50:65], v[106:109], v[130:133], v[50:65]
	s_waitcnt lgkmcnt(8)
	v_mfma_f32_32x32x16_bf16 v[34:49], v[110:113], v[130:133], v[34:49]
	s_waitcnt lgkmcnt(6)
	v_mfma_f32_32x32x16_bf16 v[18:33], v[114:117], v[136:139], v[18:33]
	s_waitcnt lgkmcnt(4)
	v_mfma_f32_32x32x16_bf16 v[2:17], v[118:121], v[136:139], v[2:17]
	s_waitcnt lgkmcnt(2)
	v_mfma_f32_32x32x16_bf16 v[18:33], v[122:125], v[130:133], v[18:33]
	s_waitcnt lgkmcnt(0)
	v_mfma_f32_32x32x16_bf16 v[2:17], v[126:129], v[130:133], v[2:17]
	s_and_b64 s[80:81], s[84:85], exec
	s_cselect_b32 s80, 0, s78
	s_mov_b64 s[84:85], 0

.LBB0_865:
	s_ashr_i32 s80, s68, 31
	s_lshr_b32 s80, s80, 30
	s_add_i32 s80, s68, s80
	s_add_i32 s78, s68, -4
	s_and_b32 s81, s80, -4
	s_max_i32 s81, s78, s81
	s_cmp_lt_i32 s73, s81
	s_cselect_b64 vcc, -1, 0
	s_or_b64 s[84:85], s[84:85], vcc
	s_cmp_gt_i32 s73, s68
	s_cselect_b64 vcc, -1, 0
	s_or_b64 vcc, vcc, s[84:85]
	s_mov_b64 s[84:85], -1
	s_and_b64 vcc, exec, vcc
	s_cbranch_vccnz .LBB0_874
	s_mul_i32 s81, s73, 0xcd
	s_bfe_u32 s81, s81, 0x6000a
	s_mul_i32 s81, s81, 5
	s_sub_i32 s81, s73, s81
	s_and_b32 s81, s81, 0xff
	s_lshl_b32 s81, s81, 14
	s_add_i32 s81, s81, 0
	v_add_u32_e32 v220, s81, v171
	v_add_u32_e32 v221, v220, v175
	ds_read_b128 v[66:69], v221
	ds_read_b128 v[98:101], v219
	v_add_u32_e32 v222, v220, v176
	ds_read_b128 v[70:73], v222
	ds_read_b128 v[102:105], v224
	v_add_u32_e32 v221, v220, v177
	ds_read_b128 v[74:77], v221
	ds_read_b128 v[106:109], v225
	v_add_u32_e32 v222, v220, v178
	ds_read_b128 v[78:81], v222
	ds_read_b128 v[110:113], v226
	v_add_u32_e32 v221, v220, v180
	ds_read_b128 v[82:85], v221
	ds_read_b128 v[114:117], v227
	v_add_u32_e32 v222, v220, v181
	ds_read_b128 v[86:89], v222
	ds_read_b128 v[118:121], v228
	s_waitcnt lgkmcnt(10)
	v_mfma_f32_32x32x16_bf16 v[130:145], v[66:69], v[98:101], 0
	v_add_u32_e32 v221, v220, v182
	ds_read_b128 v[90:93], v221
	ds_read_b128 v[122:125], v229
	s_waitcnt lgkmcnt(10)
	v_mfma_f32_32x32x16_bf16 v[130:145], v[70:73], v[102:105], v[130:145]
	v_add_u32_e32 v222, v220, v183
	ds_read_b128 v[94:97], v222
	ds_read_b128 v[126:129], v230
	s_waitcnt lgkmcnt(10)
	v_mfma_f32_32x32x16_bf16 v[130:145], v[74:77], v[106:109], v[130:145]
	s_waitcnt lgkmcnt(8)
	v_mfma_f32_32x32x16_bf16 v[130:145], v[78:81], v[110:113], v[130:145]
	s_waitcnt lgkmcnt(6)
	v_mfma_f32_32x32x16_bf16 v[130:145], v[82:85], v[114:117], v[130:145]
	s_waitcnt lgkmcnt(4)
	v_mfma_f32_32x32x16_bf16 v[130:145], v[86:89], v[118:121], v[130:145]
	s_waitcnt lgkmcnt(2)
	v_mfma_f32_32x32x16_bf16 v[130:145], v[90:93], v[122:125], v[130:145]
	s_cmp_lg_u32 s73, s78
	s_waitcnt lgkmcnt(0)
	v_mfma_f32_32x32x16_bf16 v[130:145], v[94:97], v[126:129], v[130:145]
	v_add_u32_e32 v69, s81, v173
	v_add3_u32 v70, v69, v185, v186
	ds_read_b64_tr_b16 v[98:99], v70 offset:8192
	v_add3_u32 v71, v69, v187, v188
	ds_read_b64_tr_b16 v[100:101], v71 offset:8192
	v_add3_u32 v70, v69, v185, v191
	ds_read_b64_tr_b16 v[102:103], v70 offset:8192
	v_add3_u32 v71, v69, v187, v192
	ds_read_b64_tr_b16 v[104:105], v71 offset:8192
	v_add3_u32 v70, v69, v184, v186
	ds_read_b64_tr_b16 v[106:107], v70 offset:8192
	v_add3_u32 v71, v69, v189, v190
	ds_read_b64_tr_b16 v[108:109], v71 offset:8192
	v_add3_u32 v70, v69, v184, v191
	ds_read_b64_tr_b16 v[110:111], v70 offset:8192
	v_add3_u32 v71, v69, v189, v193
	ds_read_b64_tr_b16 v[112:113], v71 offset:8192
	s_cbranch_scc1 .LBB0_868
	s_nop 10
	v_cndmask_b32_e64 v130, v130, v216, s[4:5]
	v_cndmask_b32_e64 v131, v131, v216, s[6:7]
	v_cndmask_b32_e64 v132, v132, v216, s[8:9]
	v_cndmask_b32_e64 v133, v133, v216, s[10:11]
	v_cndmask_b32_e64 v134, v134, v216, s[12:13]
	v_cndmask_b32_e64 v135, v135, v216, s[14:15]
	v_cndmask_b32_e64 v136, v136, v216, s[16:17]
	v_cndmask_b32_e64 v137, v137, v216, s[18:19]
	v_cndmask_b32_e64 v138, v138, v216, s[20:21]
	v_cndmask_b32_e64 v139, v139, v216, s[22:23]
	v_cndmask_b32_e64 v140, v140, v216, s[24:25]
	v_cndmask_b32_e64 v141, v141, v216, s[26:27]
	v_cndmask_b32_e64 v142, v142, v216, s[28:29]
	v_cndmask_b32_e64 v143, v143, v216, s[30:31]
	v_cndmask_b32_e64 v144, v144, v216, s[34:35]
	v_cndmask_b32_e64 v145, v145, v216, s[36:37]

.LBB0_872:
.LBB0_873:
	v_sub_f32_e32 v130, v130, v235
	v_exp_f32_e32 v130, v130
	v_sub_f32_e32 v131, v131, v235
	v_exp_f32_e32 v131, v131
	v_sub_f32_e32 v132, v132, v235
	v_exp_f32_e32 v132, v132
	v_sub_f32_e32 v133, v133, v235
	v_exp_f32_e32 v133, v133
	v_sub_f32_e32 v134, v134, v235
	v_add_f32_e32 v220, 0, v130
	v_exp_f32_e32 v221, v134
	v_add_f32_e32 v220, v131, v220
	v_add_f32_e32 v220, v132, v220
	v_sub_f32_e32 v135, v135, v235
	v_add_f32_e32 v220, v133, v220
	v_exp_f32_e32 v135, v135
	v_sub_f32_e32 v136, v136, v235
	v_add_f32_e32 v134, v221, v220
	v_exp_f32_e32 v220, v136
	v_sub_f32_e32 v136, v137, v235
	v_exp_f32_e32 v222, v136
	v_sub_f32_e32 v136, v138, v235
	v_exp_f32_e32 v223, v136
	v_sub_f32_e32 v136, v139, v235
	v_add_f32_e32 v134, v135, v134
	v_exp_f32_e32 v236, v136
	v_sub_f32_e32 v136, v140, v235
	v_add_f32_e32 v134, v220, v134
	v_exp_f32_e32 v140, v136
	v_sub_f32_e32 v136, v141, v235
	v_add_f32_e32 v134, v222, v134
	v_exp_f32_e32 v141, v136
	v_sub_f32_e32 v136, v142, v235
	v_add_f32_e32 v134, v223, v134
	v_exp_f32_e32 v142, v136
	v_sub_f32_e32 v136, v143, v235
	v_add_f32_e32 v134, v236, v134
	v_exp_f32_e32 v143, v136
	v_sub_f32_e32 v136, v144, v235
	v_add_f32_e32 v134, v140, v134
	v_exp_f32_e32 v144, v136
	v_sub_f32_e32 v136, v145, v235
	v_add_f32_e32 v134, v141, v134
	v_exp_f32_e32 v145, v136
	v_add_f32_e32 v134, v142, v134
	v_add_f32_e32 v134, v143, v134
	v_add_f32_e32 v134, v144, v134
	v_add_f32_e32 v134, v145, v134
	v_cvt_pk_bf16_f32 v136, v130, v131
	v_cvt_pk_bf16_f32 v137, v132, v133
	v_cvt_pk_bf16_f32 v138, v221, v135
	v_cvt_pk_bf16_f32 v139, v220, v222
	v_cvt_pk_bf16_f32 v130, v223, v236
	v_cvt_pk_bf16_f32 v131, v140, v141
	v_cvt_pk_bf16_f32 v132, v142, v143
	v_cvt_pk_bf16_f32 v133, v144, v145
	v_fmac_f32_e32 v134, v234, v146
	s_nop 1
	s_waitcnt lgkmcnt(8)
	v_mfma_f32_32x32x16_bf16 v[50:65], v[98:101], v[136:139], v[50:65]
	s_waitcnt lgkmcnt(8)
	v_mfma_f32_32x32x16_bf16 v[34:49], v[102:105], v[136:139], v[34:49]
	s_waitcnt lgkmcnt(8)
	v_mfma_f32_32x32x16_bf16 v[50:65], v[106:109], v[130:133], v[50:65]
	s_waitcnt lgkmcnt(8)
	v_mfma_f32_32x32x16_bf16 v[34:49], v[110:113], v[130:133], v[34:49]
	s_waitcnt lgkmcnt(6)
	v_mfma_f32_32x32x16_bf16 v[18:33], v[114:117], v[136:139], v[18:33]
	s_waitcnt lgkmcnt(4)
	v_mfma_f32_32x32x16_bf16 v[2:17], v[118:121], v[136:139], v[2:17]
	s_waitcnt lgkmcnt(2)
	v_mfma_f32_32x32x16_bf16 v[18:33], v[122:125], v[130:133], v[18:33]
	s_waitcnt lgkmcnt(0)
	v_mfma_f32_32x32x16_bf16 v[2:17], v[126:129], v[130:133], v[2:17]
	s_and_b64 s[84:85], s[84:85], exec
	s_cselect_b32 s81, 0, s79
	s_mov_b64 s[84:85], 0
